# nca kernels: the lgkmcnt(0) that guarded the old bpermute reduction moved down to the first PV MFMA so the 56 softmax VALU no longer wait for the prefetched V fragments
# baseline (speedup 1.0000x reference)
.LBB1_16:
	s_or_b64 exec, exec, s[2:3]
	s_movk_i32 s2, 0x168
	s_waitcnt vmcnt(4)
	v_and_b32_e32 v39, 63, v0
	v_and_b32_e32 v40, 15, v0
	v_lshlrev_b32_e32 v26, 3, v50
	v_cmp_gt_u32_e32 vcc, s2, v0
	s_and_saveexec_b64 s[2:3], vcc
	s_movk_i32 s4, 0xa0
	v_mad_u32_u24 v27, v0, s4, 0
	v_mov_b32_e32 v28, 0x3c00
	ds_write_b16 v27, v28 offset:144
	s_or_b64 exec, exec, s[2:3]
	v_lshlrev_b32_e32 v38, 2, v50
	v_or_b32_e32 v28, s21, v63
	v_add_u32_e32 v29, v28, v38
	v_sub_u32_e32 v30, v38, v61
	s_movk_i32 s7, 0x80
	v_cmp_gt_u32_e64 s[2:3], 11, v30
	v_cmp_gt_u32_e64 s[4:5], s7, v29
	v_or_b32_e32 v29, 1, v38
	s_and_b64 s[2:3], s[2:3], s[4:5]
	v_mov_b32_e32 v111, 0xff800000
	v_add_u32_e32 v30, v28, v29
	v_sub_u32_e32 v29, v29, v61
	v_cndmask_b32_e64 v112, v111, 0, s[2:3]
	v_cmp_gt_u32_e64 s[2:3], 11, v29
	v_cmp_gt_u32_e64 s[4:5], s7, v30
	v_or_b32_e32 v29, 2, v38
	v_lshrrev_b32_e32 v110, 8, v0
	s_and_b64 s[2:3], s[2:3], s[4:5]
	v_add_u32_e32 v30, v28, v29
	v_sub_u32_e32 v29, v29, v61
	v_cndmask_b32_e64 v113, v111, 0, s[2:3]
	v_cmp_gt_u32_e64 s[2:3], 11, v29
	v_or_b32_e32 v29, 3, v38
	v_mad_u32_u24 v41, v110, 7, v62
	v_cmp_gt_u32_e64 s[4:5], s7, v30
	v_add_u32_e32 v28, v28, v29
	v_mad_u32_u24 v98, v41, 20, v63
	s_and_b64 s[2:3], s[2:3], s[4:5]
	v_cmp_gt_u32_e64 s[4:5], s7, v28
	v_add_u32_e32 v28, v98, v40
	s_movk_i32 s6, 0xa0
	v_mul_lo_u32 v28, v28, s6
	v_add_u32_e32 v99, 0, v28
	v_mul_u32_u24_e32 v27, 7, v110
	v_sub_u32_e32 v29, v29, v61
	v_lshl_add_u32 v94, v26, 1, v99
	s_waitcnt lgkmcnt(0)
	s_barrier
	v_cndmask_b32_e64 v114, v111, 0, s[2:3]
	v_cmp_gt_u32_e64 s[2:3], 11, v29
	ds_read_b128 v[26:29], v94
	s_and_b64 s[2:3], s[2:3], s[4:5]
	ds_read_b128 v[34:37], v94 offset:64
	v_cndmask_b32_e64 v115, v111, 0, s[2:3]
	v_cndmask_b32_e64 v30, v111, v112, s[44:45]
	v_cndmask_b32_e64 v33, v111, v115, s[44:45]
	v_cndmask_b32_e64 v32, v111, v114, s[44:45]
	v_cndmask_b32_e64 v31, v111, v113, s[44:45]
	v_cmp_gt_u32_e32 vcc, 16, v39
	v_add_u32_e32 v98, v98, v38
	s_waitcnt lgkmcnt(1)
	v_mfma_f32_16x16x32_f16 v[30:33], v[26:29], v[10:13], v[30:33]
	ds_read_b128 v[42:45], v99 offset:128
	ds_read_b128 v[46:49], v94 offset:3200
	v_cndmask_b32_e32 v29, 0, v25, vcc
	s_waitcnt lgkmcnt(2)
	v_mfma_f32_16x16x32_f16 v[30:33], v[34:37], v[2:5], v[30:33]
	v_cndmask_b32_e32 v28, 0, v24, vcc
	v_cndmask_b32_e32 v27, 0, v23, vcc
	v_cndmask_b32_e32 v26, 0, v22, vcc
	ds_read_b128 v[34:37], v94 offset:3264
	ds_read_b128 v[50:53], v99 offset:3328
	s_waitcnt lgkmcnt(3)
	v_mfma_f32_16x16x32_f16 v[22:25], v[42:45], v[26:29], v[30:33]
	ds_read_b128 v[42:45], v94 offset:6400
	ds_read_b128 v[62:65], v94 offset:6464
	v_or_b32_e32 v98, v98, v1
	v_cndmask_b32_e64 v30, v111, v112, s[46:47]
	v_cndmask_b32_e64 v33, v111, v115, s[46:47]
	v_cndmask_b32_e64 v32, v111, v114, s[46:47]
	v_cndmask_b32_e64 v31, v111, v113, s[46:47]
	v_mul_lo_u32 v98, v98, s6
	v_lshlrev_b32_e32 v61, 3, v61
	s_waitcnt lgkmcnt(4)
	v_mfma_f32_16x16x32_f16 v[30:33], v[46:49], v[10:13], v[30:33]
	ds_read_b128 v[46:49], v99 offset:6528
	ds_read_b128 v[66:69], v94 offset:9600
	v_add3_u32 v61, 0, v98, v61
	s_waitcnt lgkmcnt(5)
	v_mfma_f32_16x16x32_f16 v[30:33], v[34:37], v[2:5], v[30:33]
	v_cndmask_b32_e64 v34, v111, v112, s[48:49]
	v_cndmask_b32_e64 v37, v111, v115, s[48:49]
	v_cndmask_b32_e64 v36, v111, v114, s[48:49]
	v_cndmask_b32_e64 v35, v111, v113, s[48:49]
	ds_read_b128 v[70:73], v94 offset:9664
	ds_read_b128 v[74:77], v99 offset:9728
	s_waitcnt lgkmcnt(6)
	v_mfma_f32_16x16x32_f16 v[30:33], v[50:53], v[26:29], v[30:33]
	ds_read_b128 v[50:53], v94 offset:12800
	ds_read_b128 v[78:81], v94 offset:12864
	s_waitcnt lgkmcnt(7)
	v_mfma_f32_16x16x32_f16 v[34:37], v[42:45], v[10:13], v[34:37]
	ds_read_b128 v[42:45], v99 offset:12928
	ds_read_b128 v[82:85], v94 offset:16000
	s_waitcnt lgkmcnt(8)
	v_mfma_f32_16x16x32_f16 v[34:37], v[62:65], v[2:5], v[34:37]
	ds_read_b128 v[62:65], v94 offset:16064
	ds_read_b128 v[86:89], v99 offset:16128
	v_mul_u32_u24_e32 v128, 0xa0, v60
	s_waitcnt lgkmcnt(9)
	v_mfma_f32_16x16x32_f16 v[34:37], v[46:49], v[26:29], v[34:37]
	v_cndmask_b32_e64 v46, v111, v112, s[50:51]
	v_cndmask_b32_e64 v49, v111, v115, s[50:51]
	v_cndmask_b32_e64 v48, v111, v114, s[50:51]
	v_cndmask_b32_e64 v47, v111, v113, s[50:51]
	ds_read_b128 v[90:93], v94 offset:19200
	ds_read_b128 v[94:97], v94 offset:19264
	s_waitcnt lgkmcnt(10)
	v_mfma_f32_16x16x32_f16 v[46:49], v[66:69], v[10:13], v[46:49]
	ds_read_b128 v[66:69], v99 offset:19328
	ds_read_b64_tr_b16 v[100:101], v61 offset:3200
	v_lshlrev_b32_e32 v129, 1, v56
	s_waitcnt lgkmcnt(11)
	v_mfma_f32_16x16x32_f16 v[46:49], v[70:73], v[2:5], v[46:49]
	ds_read_b64_tr_b16 v[98:99], v61
	ds_read_b64_tr_b16 v[70:71], v61 offset:32
	s_waitcnt lgkmcnt(12)
	v_mfma_f32_16x16x32_f16 v[46:49], v[74:77], v[26:29], v[46:49]
	v_cndmask_b32_e64 v74, v111, v112, s[52:53]
	v_cndmask_b32_e64 v77, v111, v115, s[52:53]
	v_cndmask_b32_e64 v76, v111, v114, s[52:53]
	v_cndmask_b32_e64 v75, v111, v113, s[52:53]
	ds_read_b64_tr_b16 v[72:73], v61 offset:3232
	ds_read_b64_tr_b16 v[102:103], v61 offset:64
	s_waitcnt lgkmcnt(13)
	v_mfma_f32_16x16x32_f16 v[50:53], v[50:53], v[10:13], v[74:77]
	ds_read_b64_tr_b16 v[104:105], v61 offset:3264
	v_add3_u32 v128, 0, v128, v129
	s_movk_i32 s4, 0xe39
	ds_read_b64_tr_b16 v[74:75], v61 offset:96
	s_waitcnt lgkmcnt(14)
	v_mfma_f32_16x16x32_f16 v[50:53], v[78:81], v[2:5], v[50:53]
	ds_read_b64_tr_b16 v[76:77], v61 offset:3296
	ds_read_b64_tr_b16 v[78:79], v61 offset:128
	s_movk_i32 s5, 0xffee
	s_waitcnt lgkmcnt(14)
	v_mfma_f32_16x16x32_f16 v[42:45], v[42:45], v[26:29], v[50:53]
	ds_read_b64_tr_b16 v[80:81], v61 offset:3328
	ds_read_b64_tr_b16 v[106:107], v61 offset:6400
	v_cndmask_b32_e64 v50, v111, v112, s[54:55]
	v_cndmask_b32_e64 v53, v111, v115, s[54:55]
	v_cndmask_b32_e64 v52, v111, v114, s[54:55]
	v_cndmask_b32_e64 v51, v111, v113, s[54:55]
	s_nop 0
	v_mfma_f32_16x16x32_f16 v[50:53], v[82:85], v[10:13], v[50:53]
	ds_read_b64_tr_b16 v[108:109], v61 offset:9600
	ds_read_b64_tr_b16 v[82:83], v61 offset:6432
	s_waitcnt lgkmcnt(14)
	v_mfma_f32_16x16x32_f16 v[50:53], v[62:65], v[2:5], v[50:53]
	ds_read_b64_tr_b16 v[84:85], v61 offset:9632
	ds_read_b64_tr_b16 v[62:63], v61 offset:6464
	v_mfma_f32_16x16x32_f16 v[50:53], v[86:89], v[26:29], v[50:53]
	v_cndmask_b32_e64 v86, v111, v112, s[56:57]
	v_cndmask_b32_e64 v89, v111, v115, s[56:57]
	v_cndmask_b32_e64 v88, v111, v114, s[56:57]
	v_cndmask_b32_e64 v87, v111, v113, s[56:57]
	ds_read_b64_tr_b16 v[64:65], v61 offset:9664
	ds_read_b64_tr_b16 v[110:111], v61 offset:6496
	v_mfma_f32_16x16x32_f16 v[10:13], v[90:93], v[10:13], v[86:89]
	s_mov_b32 s2, 0xff800000
	ds_read_b64_tr_b16 v[112:113], v61 offset:9696
	s_nop 0
	ds_read_b64_tr_b16 v[86:87], v61 offset:6528
	v_mfma_f32_16x16x32_f16 v[2:5], v[94:97], v[2:5], v[10:13]
	ds_read_b64_tr_b16 v[88:89], v61 offset:9728
	s_nop 1
	v_max3_f32 v12, v22, s2, v23
	v_max3_f32 v12, v12, v24, v25
	v_max3_f32 v12, v12, v30, v31
	v_max3_f32 v12, v12, v32, v33
	v_max3_f32 v12, v12, v34, v35
	v_max3_f32 v12, v12, v36, v37
	v_max3_f32 v12, v12, v46, v47
	v_max3_f32 v12, v12, v48, v49
	v_mbcnt_lo_u32_b32 v13, -1, 0
	ds_read_b64_tr_b16 v[10:11], v61 offset:12800
	s_waitcnt lgkmcnt(14)
	v_mfma_f32_16x16x32_f16 v[2:5], v[66:69], v[26:29], v[2:5]
	v_max3_f32 v12, v12, v42, v43
	v_mbcnt_hi_u32_b32 v13, -1, v13
	v_max3_f32 v12, v12, v44, v45
	v_and_b32_e32 v27, 64, v13
	v_max3_f32 v12, v12, v50, v51
	v_xor_b32_e32 v26, 16, v13
	v_add_u32_e32 v27, 64, v27
	v_max3_f32 v12, v12, v52, v53
	v_cmp_lt_i32_e32 vcc, v26, v27
	v_max3_f32 v12, v12, v2, v3
	v_max3_f32 v12, v12, v4, v5
	v_mov_b32_e32 v26, v12
	s_load_dwordx2 s[2:3], s[0:1], 0x20
	s_movk_i32 s0, 0x510
	v_permlane16_swap_b32_e32 v12, v26
	v_cmp_gt_u32_e32 vcc, 11, v41
	v_mov_b32_e32 v41, 0xc80
	v_max_f32_e32 v12, v12, v26
	v_mov_b32_e32 v13, v12
	s_nop 1
	v_permlane32_swap_b32_e32 v12, v13
	s_nop 1
	v_max_f32_e32 v26, v12, v13
	v_sub_f32_e32 v29, v34, v26
	v_exp_f32_e32 v92, v29
	v_sub_f32_e32 v29, v35, v26
	v_exp_f32_e32 v93, v29
	v_sub_f32_e32 v29, v36, v26
	v_exp_f32_e32 v36, v29
	v_sub_f32_e32 v29, v37, v26
	v_exp_f32_e32 v37, v29
	v_sub_f32_e32 v29, v46, v26
	v_exp_f32_e32 v94, v29
	v_sub_f32_e32 v29, v47, v26
	v_exp_f32_e32 v95, v29
	v_sub_f32_e32 v29, v48, v26
	v_sub_f32_e32 v13, v23, v26
	v_sub_f32_e32 v23, v25, v26
	v_sub_f32_e32 v25, v31, v26
	v_exp_f32_e32 v96, v29
	v_sub_f32_e32 v29, v49, v26
	v_sub_f32_e32 v12, v22, v26
	v_sub_f32_e32 v22, v24, v26
	v_sub_f32_e32 v24, v30, v26
	v_exp_f32_e32 v27, v25
	v_sub_f32_e32 v25, v32, v26
	v_sub_f32_e32 v28, v33, v26
	v_exp_f32_e32 v97, v29
	v_sub_f32_e32 v29, v42, v26
	v_exp_f32_e32 v12, v12
	v_exp_f32_e32 v13, v13
	v_exp_f32_e32 v22, v22
	v_exp_f32_e32 v23, v23
	v_exp_f32_e32 v24, v24
	v_exp_f32_e32 v25, v25
	v_exp_f32_e32 v28, v28
	v_exp_f32_e32 v114, v29
	v_sub_f32_e32 v29, v43, v26
	v_exp_f32_e32 v115, v29
	v_sub_f32_e32 v29, v44, v26
	v_exp_f32_e32 v116, v29
	v_sub_f32_e32 v29, v45, v26
	v_exp_f32_e32 v117, v29
	v_sub_f32_e32 v29, v50, v26
	v_exp_f32_e32 v118, v29
	v_sub_f32_e32 v29, v51, v26
	v_cvt_pk_f16_f32 v25, v25, v28
	v_cvt_pk_f16_f32 v24, v24, v27
	v_cvt_pk_f16_f32 v23, v22, v23
	v_cvt_pk_f16_f32 v22, v12, v13
	v_exp_f32_e32 v119, v29
	v_cndmask_b32_e32 v41, 0, v41, vcc
	s_waitcnt lgkmcnt(0)
	v_mfma_f32_16x16x32_f16 v[28:31], v[98:101], v[22:25], 0
	ds_read_b64_tr_b16 v[12:13], v61 offset:16000
	ds_read_b64_tr_b16 v[32:33], v61 offset:12832
	v_sub_f32_e32 v27, v52, v26
	v_mfma_f32_16x16x32_f16 v[42:45], v[70:73], v[22:25], 0
	ds_read_b64_tr_b16 v[34:35], v61 offset:16032
	ds_read_b64_tr_b16 v[46:47], v61 offset:12864
	v_exp_f32_e32 v27, v27
	v_mfma_f32_16x16x32_f16 v[66:69], v[102:105], v[22:25], 0
	ds_read_b64_tr_b16 v[48:49], v61 offset:16064
	ds_read_b64_tr_b16 v[70:71], v61 offset:12896
	v_sub_f32_e32 v2, v2, v26
	v_mfma_f32_16x16x32_f16 v[74:77], v[74:77], v[22:25], 0
	ds_read_b64_tr_b16 v[72:73], v61 offset:16096
	ds_read_b64_tr_b16 v[90:91], v61 offset:12928
	v_cmp_gt_u32_e32 vcc, s0, v58
	v_mfma_f32_16x16x32_f16 v[22:25], v[78:81], v[22:25], 0
	v_cvt_pk_f16_f32 v78, v92, v93
	ds_read_b64_tr_b16 v[92:93], v61 offset:16128
	v_cvt_pk_f16_f32 v81, v96, v97
	v_cvt_pk_f16_f32 v80, v94, v95
	v_cvt_pk_f16_f32 v79, v36, v37
	v_add_u32_e32 v36, v61, v41
	v_sub_f32_e32 v37, v53, v26
	ds_read_b64_tr_b16 v[94:95], v61 offset:19200
	v_mfma_f32_16x16x32_f16 v[28:31], v[106:109], v[78:81], v[28:31]
	ds_read_b64_tr_b16 v[96:97], v36 offset:19200
	ds_read_b64_tr_b16 v[100:101], v36 offset:19232
	v_exp_f32_e32 v37, v37
	v_mfma_f32_16x16x32_f16 v[42:45], v[82:85], v[78:81], v[42:45]
	ds_read_b64_tr_b16 v[98:99], v61 offset:19232
	ds_read_b64_tr_b16 v[50:51], v61 offset:19264
	v_mfma_f32_16x16x32_f16 v[62:65], v[62:65], v[78:81], v[66:69]
	ds_read_b64_tr_b16 v[52:53], v36 offset:19264
	s_nop 1
	ds_read_b64_tr_b16 v[66:67], v61 offset:19296
	v_mfma_f32_16x16x32_f16 v[74:77], v[110:113], v[78:81], v[74:77]
	ds_read_b64_tr_b16 v[68:69], v36 offset:19296
	ds_read_b64_tr_b16 v[82:83], v61 offset:19328
	v_mfma_f32_16x16x32_f16 v[22:25], v[86:89], v[78:81], v[22:25]
	ds_read_b64_tr_b16 v[84:85], v36 offset:19328
	s_waitcnt vmcnt(2)
	v_cvt_pk_f16_f32 v21, v20, v21
	v_cvt_pk_f16_f32 v20, v18, v19
	v_cvt_pk_f16_f32 v17, v16, v17
	v_cvt_pk_f16_f32 v16, v14, v15
	ds_write_b64 v128, v[20:21] offset:57600
	v_mul_u32_u24_sdwa v18, v59, s4 dst_sel:DWORD dst_unused:UNUSED_PAD src0_sel:WORD_0 src1_sel:DWORD
	v_mul_i32_i24_sdwa v19, v18, s5 dst_sel:DWORD dst_unused:UNUSED_PAD src0_sel:WORD_1 src1_sel:DWORD
	v_mul_u32_u24_sdwa v14, v18, s6 dst_sel:DWORD dst_unused:UNUSED_PAD src0_sel:WORD_1 src1_sel:DWORD
	v_add_lshl_u32 v15, v19, v59, 3
	v_exp_f32_e32 v18, v2
	v_sub_f32_e32 v19, v3, v26
	v_sub_f32_e32 v2, v4, v26
	v_sub_f32_e32 v21, v5, v26
	v_cvt_pk_f16_f32 v81, v27, v37
	v_cvt_pk_f16_f32 v80, v118, v119
	v_cvt_pk_f16_f32 v79, v116, v117
	v_cvt_pk_f16_f32 v78, v114, v115
	v_add3_u32 v14, 0, v14, v15
	v_exp_f32_e32 v20, v2
	v_exp_f32_e32 v21, v21
	v_exp_f32_e32 v19, v19
	s_waitcnt lgkmcnt(14)
	v_mfma_f32_16x16x32_f16 v[10:13], v[10:13], v[78:81], v[28:31]
	ds_write_b64 v14, v[16:17] offset:57600
	v_mfma_f32_16x16x32_f16 v[14:17], v[32:35], v[78:81], v[42:45]
	v_mfma_f32_16x16x32_f16 v[28:31], v[46:49], v[78:81], v[62:65]
	s_nop 1
	v_mov_b32_e32 v44, 0
	v_cvt_pk_f16_f32 v43, v20, v21
	v_cvt_pk_f16_f32 v42, v18, v19
	s_waitcnt lgkmcnt(14)
	v_mfma_f32_16x16x32_f16 v[2:5], v[70:73], v[78:81], v[74:77]
	v_mov_b32_e32 v45, v44
	s_waitcnt lgkmcnt(12)
	v_mfma_f32_16x16x32_f16 v[32:35], v[90:93], v[78:81], v[22:25]
	s_waitcnt lgkmcnt(10)
	v_mfma_f32_16x16x32_f16 v[22:25], v[94:97], v[42:45], v[10:13]
	s_waitcnt lgkmcnt(8)
	v_mfma_f32_16x16x32_f16 v[18:21], v[98:101], v[42:45], v[14:17]
	s_waitcnt lgkmcnt(6)
	v_mfma_f32_16x16x32_f16 v[14:17], v[50:53], v[42:45], v[28:31]
	s_waitcnt lgkmcnt(4)
	v_mfma_f32_16x16x32_f16 v[10:13], v[66:69], v[42:45], v[2:5]
	s_waitcnt lgkmcnt(2)
	v_mfma_f32_16x16x32_f16 v[2:5], v[82:85], v[42:45], v[32:35]
	s_and_saveexec_b64 s[0:1], vcc
	s_cbranch_execz .LBB1_20
	v_mul_u32_u24_sdwa v27, v58, s4 dst_sel:DWORD dst_unused:UNUSED_PAD src0_sel:WORD_0 src1_sel:DWORD
	v_mul_i32_i24_sdwa v28, v27, s5 dst_sel:DWORD dst_unused:UNUSED_PAD src0_sel:WORD_1 src1_sel:DWORD
	s_waitcnt vmcnt(1)
	v_cvt_pk_f16_f32 v9, v8, v9
	v_cvt_pk_f16_f32 v8, v6, v7
	v_mul_u32_u24_sdwa v6, v27, s6 dst_sel:DWORD dst_unused:UNUSED_PAD src0_sel:WORD_1 src1_sel:DWORD
	v_add_lshl_u32 v7, v28, v58, 3
	v_add3_u32 v6, 0, v6, v7
	ds_write_b64 v6, v[8:9] offset:57600

.LBB2_16:
	s_or_b64 exec, exec, s[2:3]
	s_movk_i32 s2, 0x168
	s_waitcnt vmcnt(12)
	v_and_b32_e32 v38, 63, v0
	v_lshlrev_b32_e32 v26, 3, v50
	v_cmp_gt_u32_e32 vcc, s2, v0
	s_and_saveexec_b64 s[2:3], vcc
	s_movk_i32 s4, 0xa0
	v_mad_u32_u24 v27, v0, s4, 0
	v_mov_b32_e32 v28, 0x3c00
	ds_write_b16 v27, v28 offset:144
	s_or_b64 exec, exec, s[2:3]
	v_lshlrev_b32_e32 v39, 2, v50
	v_or_b32_e32 v28, s30, v57
	v_add_u32_e32 v29, v28, v39
	v_sub_u32_e32 v30, v39, v1
	s_movk_i32 s7, 0x80
	v_cmp_gt_u32_e64 s[2:3], 11, v30
	v_cmp_gt_u32_e64 s[4:5], s7, v29
	v_or_b32_e32 v29, 1, v39
	s_and_b64 s[2:3], s[2:3], s[4:5]
	v_mov_b32_e32 v51, 0xff800000
	v_add_u32_e32 v30, v28, v29
	v_sub_u32_e32 v29, v29, v1
	v_cndmask_b32_e64 v52, v51, 0, s[2:3]
	v_cmp_gt_u32_e64 s[2:3], 11, v29
	v_cmp_gt_u32_e64 s[4:5], s7, v30
	v_or_b32_e32 v29, 2, v39
	v_lshrrev_b32_e32 v41, 8, v0
	s_and_b64 s[2:3], s[2:3], s[4:5]
	v_add_u32_e32 v30, v28, v29
	v_sub_u32_e32 v29, v29, v1
	v_cndmask_b32_e64 v53, v51, 0, s[2:3]
	v_cmp_gt_u32_e64 s[2:3], 11, v29
	v_or_b32_e32 v29, 3, v39
	v_mad_u32_u24 v40, v41, 7, v76
	v_cmp_gt_u32_e64 s[4:5], s7, v30
	v_add_u32_e32 v28, v28, v29
	v_mad_u32_u24 v116, v40, 20, v57
	s_and_b64 s[2:3], s[2:3], s[4:5]
	v_cmp_gt_u32_e64 s[4:5], s7, v28
	v_add_u32_e32 v28, v116, v59
	s_movk_i32 s6, 0xa0
	v_mul_lo_u32 v28, v28, s6
	v_add_u32_e32 v117, 0, v28
	v_mul_u32_u24_e32 v27, 7, v41
	v_sub_u32_e32 v29, v29, v1
	v_lshl_add_u32 v112, v26, 1, v117
	s_waitcnt lgkmcnt(0)
	s_barrier
	v_cndmask_b32_e64 v128, v51, 0, s[2:3]
	v_cmp_gt_u32_e64 s[2:3], 11, v29
	ds_read_b128 v[26:29], v112
	s_and_b64 s[2:3], s[2:3], s[4:5]
	ds_read_b128 v[34:37], v112 offset:64
	v_cndmask_b32_e64 v129, v51, 0, s[2:3]
	v_cndmask_b32_e64 v30, v51, v52, s[44:45]
	v_cndmask_b32_e64 v33, v51, v129, s[44:45]
	v_cndmask_b32_e64 v32, v51, v128, s[44:45]
	v_cndmask_b32_e64 v31, v51, v53, s[44:45]
	v_cmp_gt_u32_e32 vcc, 16, v38
	v_add_u32_e32 v116, v116, v39
	s_waitcnt lgkmcnt(1)
	v_mfma_f32_16x16x32_f16 v[30:33], v[26:29], v[10:13], v[30:33]
	ds_read_b128 v[42:45], v117 offset:128
	ds_read_b128 v[46:49], v112 offset:3200
	v_cndmask_b32_e32 v29, 0, v25, vcc
	s_waitcnt lgkmcnt(2)
	v_mfma_f32_16x16x32_f16 v[30:33], v[34:37], v[2:5], v[30:33]
	v_cndmask_b32_e32 v28, 0, v24, vcc
	v_cndmask_b32_e32 v27, 0, v23, vcc
	v_cndmask_b32_e32 v26, 0, v22, vcc
	ds_read_b128 v[34:37], v112 offset:3264
	ds_read_b128 v[76:79], v117 offset:3328
	s_waitcnt lgkmcnt(3)
	v_mfma_f32_16x16x32_f16 v[22:25], v[42:45], v[26:29], v[30:33]
	ds_read_b128 v[42:45], v112 offset:6400
	ds_read_b128 v[80:83], v112 offset:6464
	v_or_b32_e32 v116, v116, v60
	v_cndmask_b32_e64 v30, v51, v52, s[46:47]
	v_cndmask_b32_e64 v33, v51, v129, s[46:47]
	v_cndmask_b32_e64 v32, v51, v128, s[46:47]
	v_cndmask_b32_e64 v31, v51, v53, s[46:47]
	v_mul_lo_u32 v116, v116, s6
	s_waitcnt lgkmcnt(4)
	v_mfma_f32_16x16x32_f16 v[30:33], v[46:49], v[10:13], v[30:33]
	ds_read_b128 v[46:49], v117 offset:6528
	ds_read_b128 v[84:87], v112 offset:9600
	s_waitcnt lgkmcnt(5)
	v_mfma_f32_16x16x32_f16 v[30:33], v[34:37], v[2:5], v[30:33]
	v_cndmask_b32_e64 v34, v51, v52, s[48:49]
	v_cndmask_b32_e64 v37, v51, v129, s[48:49]
	v_cndmask_b32_e64 v36, v51, v128, s[48:49]
	v_cndmask_b32_e64 v35, v51, v53, s[48:49]
	ds_read_b128 v[88:91], v112 offset:9664
	ds_read_b128 v[92:95], v117 offset:9728
	s_waitcnt lgkmcnt(6)
	v_mfma_f32_16x16x32_f16 v[30:33], v[76:79], v[26:29], v[30:33]
	ds_read_b128 v[76:79], v112 offset:12800
	ds_read_b128 v[96:99], v112 offset:12864
	v_mul_u32_u24_e32 v146, 0xa0, v75
	s_waitcnt lgkmcnt(7)
	v_mfma_f32_16x16x32_f16 v[34:37], v[42:45], v[10:13], v[34:37]
	ds_read_b128 v[42:45], v117 offset:12928
	ds_read_b128 v[100:103], v112 offset:16000
	v_lshlrev_b32_e32 v147, 1, v54
	s_waitcnt lgkmcnt(8)
	v_mfma_f32_16x16x32_f16 v[34:37], v[80:83], v[2:5], v[34:37]
	ds_read_b128 v[80:83], v112 offset:16064
	ds_read_b128 v[104:107], v117 offset:16128
	v_add3_u32 v146, 0, v146, v147
	s_waitcnt lgkmcnt(9)
	v_mfma_f32_16x16x32_f16 v[34:37], v[46:49], v[26:29], v[34:37]
	v_cndmask_b32_e64 v46, v51, v52, s[50:51]
	v_cndmask_b32_e64 v49, v51, v129, s[50:51]
	v_cndmask_b32_e64 v48, v51, v128, s[50:51]
	v_cndmask_b32_e64 v47, v51, v53, s[50:51]
	ds_read_b128 v[108:111], v112 offset:19200
	ds_read_b128 v[112:115], v112 offset:19264
	s_waitcnt lgkmcnt(10)
	v_mfma_f32_16x16x32_f16 v[46:49], v[84:87], v[10:13], v[46:49]
	ds_read_b128 v[84:87], v117 offset:19328
	v_lshlrev_b32_e32 v117, 3, v1
	v_add3_u32 v132, 0, v116, v117
	ds_read_b64_tr_b16 v[118:119], v132 offset:3200
	s_waitcnt lgkmcnt(11)
	v_mfma_f32_16x16x32_f16 v[46:49], v[88:91], v[2:5], v[46:49]
	ds_read_b64_tr_b16 v[116:117], v132
	ds_read_b64_tr_b16 v[88:89], v132 offset:32
	s_waitcnt lgkmcnt(12)
	v_mfma_f32_16x16x32_f16 v[46:49], v[92:95], v[26:29], v[46:49]
	v_cndmask_b32_e64 v92, v51, v52, s[52:53]
	v_cndmask_b32_e64 v95, v51, v129, s[52:53]
	v_cndmask_b32_e64 v94, v51, v128, s[52:53]
	v_cndmask_b32_e64 v93, v51, v53, s[52:53]
	ds_read_b64_tr_b16 v[90:91], v132 offset:3232
	ds_read_b64_tr_b16 v[120:121], v132 offset:64
	s_waitcnt lgkmcnt(13)
	v_mfma_f32_16x16x32_f16 v[76:79], v[76:79], v[10:13], v[92:95]
	ds_read_b64_tr_b16 v[122:123], v132 offset:3264
	s_movk_i32 s8, 0xffee
	ds_read_b64_tr_b16 v[92:93], v132 offset:96
	s_waitcnt lgkmcnt(14)
	v_mfma_f32_16x16x32_f16 v[76:79], v[96:99], v[2:5], v[76:79]
	ds_read_b64_tr_b16 v[94:95], v132 offset:3296
	ds_read_b64_tr_b16 v[96:97], v132 offset:128
	s_waitcnt lgkmcnt(14)
	v_mfma_f32_16x16x32_f16 v[42:45], v[42:45], v[26:29], v[76:79]
	ds_read_b64_tr_b16 v[98:99], v132 offset:3328
	ds_read_b64_tr_b16 v[124:125], v132 offset:6400
	s_movk_i32 s4, 0x510
	v_cndmask_b32_e64 v76, v51, v52, s[54:55]
	v_cndmask_b32_e64 v79, v51, v129, s[54:55]
	v_cndmask_b32_e64 v78, v51, v128, s[54:55]
	v_cndmask_b32_e64 v77, v51, v53, s[54:55]
	s_nop 0
	v_mfma_f32_16x16x32_f16 v[76:79], v[100:103], v[10:13], v[76:79]
	ds_read_b64_tr_b16 v[126:127], v132 offset:9600
	ds_read_b64_tr_b16 v[100:101], v132 offset:6432
	s_waitcnt lgkmcnt(14)
	v_mfma_f32_16x16x32_f16 v[76:79], v[80:83], v[2:5], v[76:79]
	ds_read_b64_tr_b16 v[102:103], v132 offset:9632
	ds_read_b64_tr_b16 v[80:81], v132 offset:6464
	v_mfma_f32_16x16x32_f16 v[76:79], v[104:107], v[26:29], v[76:79]
	v_cndmask_b32_e64 v104, v51, v52, s[56:57]
	v_cndmask_b32_e64 v107, v51, v129, s[56:57]
	v_cndmask_b32_e64 v106, v51, v128, s[56:57]
	v_cndmask_b32_e64 v105, v51, v53, s[56:57]
	ds_read_b64_tr_b16 v[82:83], v132 offset:9664
	ds_read_b64_tr_b16 v[128:129], v132 offset:6496
	v_mfma_f32_16x16x32_f16 v[10:13], v[108:111], v[10:13], v[104:107]
	s_mov_b32 s2, 0xff800000
	ds_read_b64_tr_b16 v[130:131], v132 offset:9696
	s_movk_i32 s7, 0xe39
	ds_read_b64_tr_b16 v[104:105], v132 offset:6528
	v_mfma_f32_16x16x32_f16 v[2:5], v[112:115], v[2:5], v[10:13]
	ds_read_b64_tr_b16 v[106:107], v132 offset:9728
	s_nop 1
	v_max3_f32 v12, v22, s2, v23
	v_max3_f32 v12, v12, v24, v25
	v_max3_f32 v12, v12, v30, v31
	v_max3_f32 v12, v12, v32, v33
	v_max3_f32 v12, v12, v34, v35
	v_max3_f32 v12, v12, v36, v37
	v_max3_f32 v12, v12, v46, v47
	v_max3_f32 v12, v12, v48, v49
	v_mbcnt_lo_u32_b32 v13, -1, 0
	ds_read_b64_tr_b16 v[10:11], v132 offset:12800
	s_waitcnt lgkmcnt(14)
	v_mfma_f32_16x16x32_f16 v[2:5], v[84:87], v[26:29], v[2:5]
	v_max3_f32 v12, v12, v42, v43
	v_mbcnt_hi_u32_b32 v13, -1, v13
	v_max3_f32 v12, v12, v44, v45
	v_and_b32_e32 v27, 64, v13
	v_max3_f32 v12, v12, v76, v77
	v_xor_b32_e32 v26, 16, v13
	v_add_u32_e32 v27, 64, v27
	v_max3_f32 v12, v12, v78, v79
	v_cmp_lt_i32_e32 vcc, v26, v27
	v_max3_f32 v12, v12, v2, v3
	v_max3_f32 v12, v12, v4, v5
	v_mov_b32_e32 v26, v12
	v_cmp_lt_u32_e64 s[2:3], 15, v38
	s_nop 0
	v_permlane16_swap_b32_e32 v12, v26
	v_cmp_gt_u32_e32 vcc, 11, v40
	s_nop 0
	v_max_f32_e32 v12, v12, v26
	v_mov_b32_e32 v13, v12
	s_nop 1
	v_permlane32_swap_b32_e32 v12, v13
	s_nop 1
	v_max_f32_e32 v28, v12, v13
	v_sub_f32_e32 v12, v22, v28
	v_sub_f32_e32 v22, v24, v28
	v_sub_f32_e32 v24, v30, v28
	v_sub_f32_e32 v30, v35, v28
	v_exp_f32_e32 v41, v30
	v_sub_f32_e32 v30, v36, v28
	v_exp_f32_e32 v51, v30
	v_sub_f32_e32 v30, v37, v28
	v_exp_f32_e32 v52, v30
	v_sub_f32_e32 v30, v46, v28
	v_exp_f32_e32 v53, v30
	v_sub_f32_e32 v30, v47, v28
	v_exp_f32_e32 v110, v30
	v_sub_f32_e32 v30, v48, v28
	v_sub_f32_e32 v13, v23, v28
	v_sub_f32_e32 v23, v25, v28
	v_sub_f32_e32 v25, v31, v28
	v_exp_f32_e32 v111, v30
	v_sub_f32_e32 v30, v49, v28
	v_exp_f32_e32 v26, v25
	v_sub_f32_e32 v25, v32, v28
	v_sub_f32_e32 v27, v33, v28
	v_exp_f32_e32 v112, v30
	v_sub_f32_e32 v30, v42, v28
	v_exp_f32_e32 v12, v12
	v_exp_f32_e32 v13, v13
	v_exp_f32_e32 v22, v22
	v_exp_f32_e32 v23, v23
	v_exp_f32_e32 v24, v24
	v_exp_f32_e32 v25, v25
	v_exp_f32_e32 v27, v27
	v_exp_f32_e32 v133, v30
	v_sub_f32_e32 v30, v43, v28
	v_exp_f32_e32 v134, v30
	v_sub_f32_e32 v30, v44, v28
	v_exp_f32_e32 v135, v30
	v_sub_f32_e32 v30, v45, v28
	v_sub_f32_e32 v29, v34, v28
	v_exp_f32_e32 v136, v30
	v_sub_f32_e32 v30, v76, v28
	v_exp_f32_e32 v29, v29
	v_exp_f32_e32 v137, v30
	v_sub_f32_e32 v30, v77, v28
	v_cvt_pk_f16_f32 v25, v25, v27
	v_cvt_pk_f16_f32 v24, v24, v26
	v_cvt_pk_f16_f32 v23, v22, v23
	v_cvt_pk_f16_f32 v22, v12, v13
	v_exp_f32_e32 v138, v30
	v_mov_b32_e32 v27, 0xc80
	s_waitcnt lgkmcnt(0)
	v_mfma_f32_16x16x32_f16 v[30:33], v[116:119], v[22:25], 0
	ds_read_b64_tr_b16 v[12:13], v132 offset:16000
	ds_read_b64_tr_b16 v[34:35], v132 offset:12832
	v_cndmask_b32_e32 v27, 0, v27, vcc
	v_mfma_f32_16x16x32_f16 v[42:45], v[88:91], v[22:25], 0
	ds_read_b64_tr_b16 v[36:37], v132 offset:16032
	ds_read_b64_tr_b16 v[46:47], v132 offset:12864
	v_sub_f32_e32 v26, v78, v28
	v_mfma_f32_16x16x32_f16 v[84:87], v[120:123], v[22:25], 0
	ds_read_b64_tr_b16 v[48:49], v132 offset:16064
	ds_read_b64_tr_b16 v[88:89], v132 offset:12896
	v_add_u32_e32 v27, v132, v27
	v_mfma_f32_16x16x32_f16 v[92:95], v[92:95], v[22:25], 0
	ds_read_b64_tr_b16 v[90:91], v132 offset:16096
	ds_read_b64_tr_b16 v[108:109], v132 offset:12928
	v_exp_f32_e32 v26, v26
	v_mfma_f32_16x16x32_f16 v[22:25], v[96:99], v[22:25], 0
	v_cvt_pk_f16_f32 v99, v111, v112
	v_cvt_pk_f16_f32 v98, v53, v110
	ds_read_b64_tr_b16 v[110:111], v132 offset:16128
	v_cvt_pk_f16_f32 v97, v51, v52
	v_cvt_pk_f16_f32 v96, v29, v41
	v_sub_f32_e32 v29, v79, v28
	ds_read_b64_tr_b16 v[112:113], v132 offset:19200
	v_mfma_f32_16x16x32_f16 v[30:33], v[124:127], v[96:99], v[30:33]
	ds_read_b64_tr_b16 v[114:115], v27 offset:19200
	ds_read_b64_tr_b16 v[118:119], v27 offset:19232
	v_exp_f32_e32 v29, v29
	v_mfma_f32_16x16x32_f16 v[40:43], v[100:103], v[96:99], v[42:45]
	ds_read_b64_tr_b16 v[116:117], v132 offset:19232
	ds_read_b64_tr_b16 v[76:77], v132 offset:19264
	v_sub_f32_e32 v2, v2, v28
	v_mfma_f32_16x16x32_f16 v[80:83], v[80:83], v[96:99], v[84:87]
	ds_read_b64_tr_b16 v[78:79], v27 offset:19264
	v_cmp_gt_u32_e32 vcc, s4, v61
	s_nop 0
	ds_read_b64_tr_b16 v[84:85], v132 offset:19296
	v_mfma_f32_16x16x32_f16 v[92:95], v[128:131], v[96:99], v[92:95]
	ds_read_b64_tr_b16 v[86:87], v27 offset:19296
	ds_read_b64_tr_b16 v[100:101], v132 offset:19328
	v_mfma_f32_16x16x32_f16 v[22:25], v[104:107], v[96:99], v[22:25]
	ds_read_b64_tr_b16 v[102:103], v27 offset:19328
	s_waitcnt vmcnt(10)
	v_cvt_pk_f16_f32 v21, v20, v21
	v_cvt_pk_f16_f32 v20, v18, v19
	v_cvt_pk_f16_f32 v17, v16, v17
	v_cvt_pk_f16_f32 v16, v14, v15
	ds_write_b64 v146, v[20:21] offset:57600
	v_mul_u32_u24_sdwa v18, v62, s7 dst_sel:DWORD dst_unused:UNUSED_PAD src0_sel:WORD_0 src1_sel:DWORD
	v_mul_i32_i24_sdwa v19, v18, s8 dst_sel:DWORD dst_unused:UNUSED_PAD src0_sel:WORD_1 src1_sel:DWORD
	v_mul_u32_u24_sdwa v14, v18, s6 dst_sel:DWORD dst_unused:UNUSED_PAD src0_sel:WORD_1 src1_sel:DWORD
	v_add_lshl_u32 v15, v19, v62, 3
	v_exp_f32_e32 v18, v2
	v_sub_f32_e32 v19, v3, v28
	v_sub_f32_e32 v2, v4, v28
	v_sub_f32_e32 v21, v5, v28
	v_cvt_pk_f16_f32 v99, v26, v29
	v_cvt_pk_f16_f32 v98, v137, v138
	v_cvt_pk_f16_f32 v97, v135, v136
	v_cvt_pk_f16_f32 v96, v133, v134
	v_add3_u32 v14, 0, v14, v15
	v_exp_f32_e32 v20, v2
	v_exp_f32_e32 v21, v21
	v_exp_f32_e32 v19, v19
	s_waitcnt lgkmcnt(14)
	v_mfma_f32_16x16x32_f16 v[10:13], v[10:13], v[96:99], v[30:33]
	ds_write_b64 v14, v[16:17] offset:57600
	v_mfma_f32_16x16x32_f16 v[14:17], v[34:37], v[96:99], v[40:43]
	v_mfma_f32_16x16x32_f16 v[30:33], v[46:49], v[96:99], v[80:83]
	s_nop 1
	v_mov_b32_e32 v42, 0
	v_cvt_pk_f16_f32 v41, v20, v21
	v_cvt_pk_f16_f32 v40, v18, v19
	s_waitcnt lgkmcnt(14)
	v_mfma_f32_16x16x32_f16 v[2:5], v[88:91], v[96:99], v[92:95]
	v_mov_b32_e32 v43, v42
	s_waitcnt lgkmcnt(12)
	v_mfma_f32_16x16x32_f16 v[34:37], v[108:111], v[96:99], v[22:25]
	s_waitcnt lgkmcnt(10)
	v_mfma_f32_16x16x32_f16 v[22:25], v[112:115], v[40:43], v[10:13]
	s_waitcnt lgkmcnt(8)
	v_mfma_f32_16x16x32_f16 v[18:21], v[116:119], v[40:43], v[14:17]
	s_waitcnt lgkmcnt(6)
	v_mfma_f32_16x16x32_f16 v[14:17], v[76:79], v[40:43], v[30:33]
	s_waitcnt lgkmcnt(4)
	v_mfma_f32_16x16x32_f16 v[10:13], v[84:87], v[40:43], v[2:5]
	s_waitcnt lgkmcnt(2)
	v_mfma_f32_16x16x32_f16 v[2:5], v[100:103], v[40:43], v[34:37]
	s_and_saveexec_b64 s[4:5], vcc
	s_cbranch_execz .LBB2_20
	v_mul_u32_u24_sdwa v26, v61, s7 dst_sel:DWORD dst_unused:UNUSED_PAD src0_sel:WORD_0 src1_sel:DWORD
	v_mul_i32_i24_sdwa v27, v26, s8 dst_sel:DWORD dst_unused:UNUSED_PAD src0_sel:WORD_1 src1_sel:DWORD
	s_waitcnt vmcnt(8)
	v_cvt_pk_f16_f32 v9, v8, v9
	v_cvt_pk_f16_f32 v8, v6, v7
	v_mul_u32_u24_sdwa v6, v26, s6 dst_sel:DWORD dst_unused:UNUSED_PAD src0_sel:WORD_1 src1_sel:DWORD
	v_add_lshl_u32 v7, v27, v61, 3
	v_add3_u32 v6, 0, v6, v7
	ds_write_b64 v6, v[8:9] offset:57600
